# baseline (speedup 1.0000x reference)
.Lp_top:
	s_setprio 2
	s_cmp_eq_u32 s52, 1
	s_cbranch_scc1 .Lp_done
	v_readfirstlane_b32 s35, v12
	v_readfirstlane_b32 s36, v13
	s_nop 1
	v_mov_b32_e32 v11, s35
	v_mov_b32_e32 v14, s36
	v_cndmask_b32_e64 v12, v11, v14, s[54:55]
	v_cndmask_b32_e64 v13, v11, v14, s[56:57]
	v_lshl_add_u32 v12, v12, 3, v61
	v_lshl_add_u32 v14, v13, 4, v62
	ds_read_b64 v[2:3], v12
	ds_read_b128 v[4:7], v14
	s_mov_b64 exec, 1
	ds_add_rtn_u32 v10, v59, v60
	s_mov_b64 exec, -1
	v_mad_u32_u24 v9, v13, s49, v58
	v_mov_b32_e32 v8, v56
	s_waitcnt lgkmcnt(1)
	v_add_u32_e32 v2, v2, v55
	v_and_b32_e32 v3, v3, v63
	s_nop 0
	v_readlane_b32 s41, v3, 0
	v_readlane_b32 s42, v3, 4
	s_max_u32 s43, s41, s42
	s_cmp_eq_u32 s43, 0
	s_cbranch_scc1 .Lp_zero
	ds_read_b64 v[36:37], v2
	v_cmp_gt_u32_e32 vcc, v3, v8
	v_add_u32_e32 v2, 64, v2
	v_add_u32_e32 v8, 16, v8
	v_mov_b32_e32 v33, 0x3c00
	s_waitcnt lgkmcnt(0)
	v_perm_b32 v32, v37, v36, v57
	v_cndmask_b32_e32 v33, 0, v33, vcc
	s_nop 0
	v_cndmask_b32_e32 v32, 0, v32, vcc
	s_nop 1
	v_mfma_f32_32x32x16_f16 v[96:111], v[32:35], v[64:67], 0
	v_mfma_f32_32x32x16_f16 v[112:127], v[32:35], v[68:71], 0
	v_readfirstlane_b32 s34, v10
	s_cmp_lt_u32 s34, s62
	s_cselect_b32 s45, s64, s65
	s_cselect_b32 s46, 0, s62
	s_cselect_b32 s48, s62, s63
	s_sub_u32 s47, s34, s46
	s_cmp_ge_u32 s47, s48
	s_cselect_b32 s52, 1, 0
	s_lshl_b32 s47, s47, 3
	s_add_u32 s45, s45, s47
	v_mov_b32_e32 v11, s45
	ds_read2_b32 v[12:13], v11 offset1:1
	s_setprio 0
	s_mov_b32 s45, s43
	s_min_u32 s46, s45, 16
	s_cmp_eq_u32 s46, 16
	s_cbranch_scc1 .Lf16
	s_cmp_eq_u32 s46, 15
	s_cbranch_scc1 .Lf15
	s_cmp_eq_u32 s46, 14
	s_cbranch_scc1 .Lf14
	s_cmp_eq_u32 s46, 13
	s_cbranch_scc1 .Lf13
	s_cmp_eq_u32 s46, 12
	s_cbranch_scc1 .Lf12
	s_cmp_eq_u32 s46, 11
	s_cbranch_scc1 .Lf11
	s_cmp_eq_u32 s46, 10
	s_cbranch_scc1 .Lf10
	s_cmp_eq_u32 s46, 9
	s_cbranch_scc1 .Lf9
	s_cmp_eq_u32 s46, 8
	s_cbranch_scc1 .Lf8
	s_cmp_eq_u32 s46, 7
	s_cbranch_scc1 .Lf7
	s_cmp_eq_u32 s46, 6
	s_cbranch_scc1 .Lf6
	s_cmp_eq_u32 s46, 5
	s_cbranch_scc1 .Lf5
	s_cmp_eq_u32 s46, 4
	s_cbranch_scc1 .Lf4
	s_cmp_eq_u32 s46, 3
	s_cbranch_scc1 .Lf3
	s_cmp_eq_u32 s46, 2
	s_cbranch_scc1 .Lf2

.Lp_done:
	s_setprio 0
	s_waitcnt lgkmcnt(0)
	v_xor_b32_e32 v102, 16, v18
	v_lshlrev_b32_e32 v102, 2, v102
	s_branch .LBB3_67
